# M: MoE-up epilogue body regenerated by hand: 8 independent element chains per store group (no hazard nops), lin-bias+1 folded into accumulator init
# speedup vs baseline: 1.0080x; 1.0001x over previous
; template <class Epi, class Sched, bool ALIGN_EPI = false, bool SP2 = false, bool GATHER = false, bool HALFM = false>
; __device__ __forceinline__ void gemm_phase(PG8_LAS unsigned char* lds, const int Kdim, const Sched& S, const Epi& E) {
;     ...
;     f32x4 acc[2][2][4][2];
; #pragma unroll
;     for (int a = 0; a < 2; ++a)
; #pragma unroll
;         for (int b = 0; b < 2; ++b)
; #pragma unroll
;             for (int m = 0; m < 4; ++m)
; #pragma unroll
;                 for (int n = 0; n < 2; ++n) acc[a][b][m][n] = (f32x4){0.f, 0.f, 0.f, 0.f};
;     __device__ __forceinline__ void operator()(const pg8::f32x4 (&acc)[2][2][4][2], const pg8::Unit& u, int wr, int wc, int fr, int fq) const {
;     ...
;         const int colj = u.pn * 128 + wc * 32 + 8 * fq;
;         const float* bg = b_up + u.e * 2048 + colj;
;         f32x4 bgv[2], blv[2];
; #pragma unroll
;         for (int n = 0; n < 2; ++n) { bgv[n] = *(const f32x4*)(bg + 4 * n); blv[n] = *(const f32x4*)(bg + 1024 + 4 * n); }
;     ...
;                         const float g = fminf(acc[ai][0][m][n][j] + bgv[n][j], 7.f);
;                         const float l = fminf(fmaxf(acc[ai][1][m][n][j] + blv[n][j], -7.f), 7.f);
;                         const float sg = __builtin_amdgcn_rcpf(1.f + __builtin_amdgcn_exp2f(-1.702f * 1.4426950408889634f * g));
;                         a[n * 4 + j] = g * sg * (l + 1.f);
.LBB0_1696:
	v_readlane_b32 s52, v251, 31
	s_lshl_b64 s[14:15], s[20:21], 18
	v_readlane_b32 s56, v251, 35
	v_bfe_u32 v9, v2, 4, 2
	v_readlane_b32 s57, v251, 36
	s_add_u32 s37, s56, s14
	v_and_b32_e32 v8, 15, v2
	v_lshlrev_b32_e32 v10, 3, v9
	v_lshlrev_b32_e32 v9, 4, v9
	v_lshlrev_b32_e32 v2, 2, v2
	s_addc_u32 s49, s57, s15
	s_and_b32 s7, s4, 3
	v_lshl_or_b32 v169, s5, 6, v8
	v_lshl_or_b32 v8, v8, 6, v9
	s_lshl_b32 s4, s5, 13
	v_and_b32_e32 v2, 32, v2
	v_bitop3_b32 v9, v8, s4, v2 bitop3:0xde
	s_lshl_b32 s4, s7, 12
	v_bitop3_b32 v170, v8, s4, v2 bitop3:0xde
	s_add_i32 m0, s12, 0x18000
	v_lshl_add_u64 v[4:5], v[4:5], 0, s[34:35]
	v_readlane_b32 s4, v251, 8
	v_mov_b32_e32 v149, v3
	s_waitcnt vmcnt(2)
	s_barrier
	global_load_lds_dwordx4 v[4:5], off
	v_lshl_add_u64 v[4:5], v[6:7], 0, s[34:35]
	s_add_i32 m0, s12, 0x1a000
	v_readlane_b32 s5, v251, 9
	s_add_i32 s50, s12, 0x8000
	v_mov_b32_e32 v151, v3
	global_load_lds_dwordx4 v[4:5], off
	v_lshl_add_u64 v[4:5], s[4:5], 0, v[148:149]
	s_mov_b32 m0, s50
	s_add_i32 s51, s12, 0xa000
	global_load_lds_dwordx4 v[4:5], off
	v_lshl_add_u64 v[4:5], s[4:5], 0, v[150:151]
	s_add_u32 s4, s40, 0x40080
	s_mov_b32 m0, s51
	s_addc_u32 s5, s41, 0
	global_load_lds_dwordx4 v[4:5], off
	s_add_i32 m0, s12, 0x1c000
	v_lshl_add_u64 v[4:5], s[4:5], 0, v[156:157]
	global_load_lds_dwordx4 v[4:5], off
	v_lshl_add_u64 v[4:5], s[4:5], 0, v[158:159]
	s_add_i32 m0, s12, 0x1e000
	s_cmpk_lt_u32 s6, 0x100
	global_load_lds_dwordx4 v[4:5], off
	s_waitcnt vmcnt(6)
	v_readlane_b32 s53, v251, 32
	v_readlane_b32 s54, v251, 33
	v_readlane_b32 s55, v251, 34
	v_lshl_or_b32 v149, s7, 5, v10
	s_cselect_b64 s[6:7], -1, 0
	s_lshl_b32 s4, s46, 11
	s_ashr_i32 s5, s4, 31
	s_lshl_b64 s[4:5], s[4:5], 2
	v_lshl_or_b32 v136, s47, 7, v149
	s_add_u32 s4, s37, s4
	s_addc_u32 s5, s49, s5
	v_ashrrev_i32_e32 v137, 31, v136
	v_lshl_add_u64 v[136:137], v[136:137], 2, s[4:5]
	global_load_dwordx4 v[224:227], v[136:137], off
	global_load_dwordx4 v[228:231], v[136:137], off offset:16
	s_mov_b64 s[4:5], 0x1000
	v_lshl_add_u64 v[138:139], v[136:137], 0, s[4:5]
	global_load_dwordx4 v[232:235], v[138:139], off
	global_load_dwordx4 v[236:239], v[138:139], off offset:16
	s_waitcnt vmcnt(0)
	v_add_f32_e32 v4, 1.0, v236
	v_or_b32_e32 v151, 16, v169
	v_or_b32_e32 v171, 32, v169
	v_or_b32_e32 v172, 48, v169
	v_add_u32_e32 v173, 0x80, v169
	v_add_u32_e32 v174, 0x90, v169
	v_add_u32_e32 v175, 0xa0, v169
	v_add_u32_e32 v176, 0xb0, v169
	s_mov_b32 s76, 0
	v_add_u32_e32 v177, 0, v9
	v_add_f32_e32 v5, 1.0, v237
	v_add_f32_e32 v6, 1.0, v238
	v_add_f32_e32 v7, 1.0, v239
	v_add_f32_e32 v8, 1.0, v232
	v_add_f32_e32 v9, 1.0, v233
	v_add_f32_e32 v10, 1.0, v234
	v_add_f32_e32 v11, 1.0, v235
	v_add_f32_e32 v12, 1.0, v236
	v_add_f32_e32 v13, 1.0, v237
	v_add_f32_e32 v14, 1.0, v238
	v_add_f32_e32 v15, 1.0, v239
	v_add_f32_e32 v16, 1.0, v232
	v_add_f32_e32 v17, 1.0, v233
	v_add_f32_e32 v18, 1.0, v234
	v_add_f32_e32 v19, 1.0, v235
	v_add_f32_e32 v20, 1.0, v236
	v_add_f32_e32 v21, 1.0, v237
	v_add_f32_e32 v22, 1.0, v238
	v_add_f32_e32 v23, 1.0, v239
	v_add_f32_e32 v24, 1.0, v232
	v_add_f32_e32 v25, 1.0, v233
	v_add_f32_e32 v26, 1.0, v234
	v_add_f32_e32 v27, 1.0, v235
	v_add_f32_e32 v28, 1.0, v236
	v_add_f32_e32 v29, 1.0, v237
	v_add_f32_e32 v30, 1.0, v238
	v_add_f32_e32 v31, 1.0, v239
	v_add_f32_e32 v32, 1.0, v232
	v_add_f32_e32 v33, 1.0, v233
	v_add_f32_e32 v34, 1.0, v234
	v_add_f32_e32 v35, 1.0, v235
	v_mov_b32_e32 v36, v228
	v_mov_b32_e32 v37, v229
	v_mov_b32_e32 v38, v230
	v_mov_b32_e32 v39, v231
	v_mov_b32_e32 v40, v224
	v_mov_b32_e32 v41, v225
	v_mov_b32_e32 v42, v226
	v_mov_b32_e32 v43, v227
	v_mov_b32_e32 v44, v228
	v_mov_b32_e32 v45, v229
	v_mov_b32_e32 v46, v230
	v_mov_b32_e32 v47, v231
	v_mov_b32_e32 v48, v224
	v_mov_b32_e32 v49, v225
	v_mov_b32_e32 v50, v226
	v_mov_b32_e32 v51, v227
	v_mov_b32_e32 v52, v228
	v_mov_b32_e32 v53, v229
	v_mov_b32_e32 v54, v230
	v_mov_b32_e32 v55, v231
	v_mov_b32_e32 v56, v224
	v_mov_b32_e32 v57, v225
	v_mov_b32_e32 v58, v226
	v_mov_b32_e32 v59, v227
	v_mov_b32_e32 v60, v228
	v_mov_b32_e32 v61, v229
	v_mov_b32_e32 v62, v230
	v_mov_b32_e32 v63, v231
	v_mov_b32_e32 v64, v224
	v_mov_b32_e32 v65, v225
	v_mov_b32_e32 v66, v226
	v_mov_b32_e32 v67, v227
	v_add_f32_e32 v68, 1.0, v236
	v_add_f32_e32 v69, 1.0, v237
	v_add_f32_e32 v70, 1.0, v238
	v_add_f32_e32 v71, 1.0, v239
	v_add_f32_e32 v72, 1.0, v232
	v_add_f32_e32 v73, 1.0, v233
	v_add_f32_e32 v74, 1.0, v234
	v_add_f32_e32 v75, 1.0, v235
	v_add_f32_e32 v76, 1.0, v236
	v_add_f32_e32 v77, 1.0, v237
	v_add_f32_e32 v78, 1.0, v238
	v_add_f32_e32 v79, 1.0, v239
	v_add_f32_e32 v80, 1.0, v232
	v_add_f32_e32 v81, 1.0, v233
	v_add_f32_e32 v82, 1.0, v234
	v_add_f32_e32 v83, 1.0, v235
	v_add_f32_e32 v84, 1.0, v236
	v_add_f32_e32 v85, 1.0, v237
	v_add_f32_e32 v86, 1.0, v238
	v_add_f32_e32 v87, 1.0, v239
	v_add_f32_e32 v88, 1.0, v232
	v_add_f32_e32 v89, 1.0, v233
	v_add_f32_e32 v90, 1.0, v234
	v_add_f32_e32 v91, 1.0, v235
	v_add_f32_e32 v92, 1.0, v236
	v_add_f32_e32 v93, 1.0, v237
	v_add_f32_e32 v94, 1.0, v238
	v_add_f32_e32 v95, 1.0, v239
	v_add_f32_e32 v96, 1.0, v232
	v_add_f32_e32 v97, 1.0, v233
	v_add_f32_e32 v98, 1.0, v234
	v_add_f32_e32 v99, 1.0, v235
	v_mov_b32_e32 v100, v228
	v_mov_b32_e32 v101, v229
	v_mov_b32_e32 v102, v230
	v_mov_b32_e32 v103, v231
	v_mov_b32_e32 v104, v224
	v_mov_b32_e32 v105, v225
	v_mov_b32_e32 v106, v226
	v_mov_b32_e32 v107, v227
	v_mov_b32_e32 v108, v228
	v_mov_b32_e32 v109, v229
	v_mov_b32_e32 v110, v230
	v_mov_b32_e32 v111, v231
	v_mov_b32_e32 v112, v224
	v_mov_b32_e32 v113, v225
	v_mov_b32_e32 v114, v226
	v_mov_b32_e32 v115, v227
	v_mov_b32_e32 v116, v228
	v_mov_b32_e32 v117, v229
	v_mov_b32_e32 v118, v230
	v_mov_b32_e32 v119, v231
	v_mov_b32_e32 v120, v224
	v_mov_b32_e32 v121, v225
	v_mov_b32_e32 v122, v226
	v_mov_b32_e32 v123, v227
	v_mov_b32_e32 v124, v228
	v_mov_b32_e32 v125, v229
	v_mov_b32_e32 v126, v230
	v_mov_b32_e32 v127, v231
	v_mov_b32_e32 v128, v224
	v_mov_b32_e32 v129, v225
	v_mov_b32_e32 v130, v226
	v_mov_b32_e32 v131, v227
	v_readlane_b32 s58, v251, 37
	v_readlane_b32 s59, v251, 38
	v_readlane_b32 s60, v251, 39
	v_readlane_b32 s61, v251, 40
	v_readlane_b32 s62, v251, 41
	v_readlane_b32 s63, v251, 42
	v_readlane_b32 s64, v251, 43
	v_readlane_b32 s65, v251, 44
	v_readlane_b32 s66, v251, 45
	v_readlane_b32 s67, v251, 46
	s_barrier
	s_branch .LBB0_1698
; #define PG8_BAR __builtin_amdgcn_s_barrier()
; template <class Epi, class Sched, bool ALIGN_EPI = false, bool SP2 = false, bool GATHER = false, bool HALFM = false>
; __device__ __forceinline__ void gemm_phase(PG8_LAS unsigned char* lds, const int Kdim, const Sched& S, const Epi& E) {
;     ...
;         if (!has_next) break;
; #pragma unroll
;         for (int a = 0; a < 2; ++a)
; #pragma unroll
;             for (int b = 0; b < 2; ++b)
; #pragma unroll
;                 for (int m = 0; m < 4; ++m)
; #pragma unroll
;                     for (int n = 0; n < 2; ++n) acc[a][b][m][n] = (f32x4){0.f, 0.f, 0.f, 0.f};
;         cur = nxt; cA = nA; cB = nB; ++ui;
;         if constexpr (GATHER) {
; #pragma unroll
;             for (int h = 0; h < 2; ++h)
; #pragma unroll
;                 for (int i = 0; i < 2; ++i) { gc[h][i] = gn[h][i]; if (has_nn) gn[h][i] = (unsigned)ix[h][i] * (unsigned)(K * 2) + CA2[i]; } }
;         if constexpr (ALIGN_EPI) { if (wr == 1) PG8_BAR; }
.LBB0_1697:
	v_lshlrev_b32_e32 v178, 11, v178
	v_lshlrev_b32_e32 v179, 11, v179
	v_lshlrev_b32_e32 v180, 11, v180
	v_lshlrev_b32_e32 v181, 11, v181
	v_add_u32_e32 v4, v178, v165
	v_cndmask_b32_e64 v5, v166, v4, s[42:43]
	v_add_u32_e32 v4, v181, v162
	v_add_u32_e32 v2, v179, v162
	v_cndmask_b32_e64 v6, v167, v4, s[42:43]
	v_add_u32_e32 v4, v180, v165
	v_cndmask_b32_e64 v2, v163, v2, s[42:43]
	v_cndmask_b32_e64 v7, v168, v4, s[42:43]
	s_waitcnt vmcnt(8)
	v_add_f32_e32 v4, 1.0, v236
	v_mov_b32_e32 v148, v163
	v_mov_b32_e32 v150, v166
	v_mov_b32_e32 v152, v167
	v_mov_b32_e32 v154, v168
	v_mov_b32_e32 v163, v2
	v_mov_b32_e32 v166, v5
	v_mov_b32_e32 v167, v6
	v_mov_b32_e32 v168, v7
	s_mov_b32 s48, s57
	s_mov_b32 s47, s54
	s_mov_b32 s46, s52
	s_mov_b64 s[40:41], s[16:17]
	v_add_f32_e32 v5, 1.0, v237
	v_add_f32_e32 v6, 1.0, v238
	v_add_f32_e32 v7, 1.0, v239
	v_add_f32_e32 v8, 1.0, v232
	v_add_f32_e32 v9, 1.0, v233
	v_add_f32_e32 v10, 1.0, v234
	v_add_f32_e32 v11, 1.0, v235
	v_add_f32_e32 v12, 1.0, v236
	v_add_f32_e32 v13, 1.0, v237
	v_add_f32_e32 v14, 1.0, v238
	v_add_f32_e32 v15, 1.0, v239
	v_add_f32_e32 v16, 1.0, v232
	v_add_f32_e32 v17, 1.0, v233
	v_add_f32_e32 v18, 1.0, v234
	v_add_f32_e32 v19, 1.0, v235
	v_add_f32_e32 v20, 1.0, v236
	v_add_f32_e32 v21, 1.0, v237
	v_add_f32_e32 v22, 1.0, v238
	v_add_f32_e32 v23, 1.0, v239
	v_add_f32_e32 v24, 1.0, v232
	v_add_f32_e32 v25, 1.0, v233
	v_add_f32_e32 v26, 1.0, v234
	v_add_f32_e32 v27, 1.0, v235
	v_add_f32_e32 v28, 1.0, v236
	v_add_f32_e32 v29, 1.0, v237
	v_add_f32_e32 v30, 1.0, v238
	v_add_f32_e32 v31, 1.0, v239
	v_add_f32_e32 v32, 1.0, v232
	v_add_f32_e32 v33, 1.0, v233
	v_add_f32_e32 v34, 1.0, v234
	v_add_f32_e32 v35, 1.0, v235
	v_mov_b32_e32 v36, v228
	v_mov_b32_e32 v37, v229
	v_mov_b32_e32 v38, v230
	v_mov_b32_e32 v39, v231
	v_mov_b32_e32 v40, v224
	v_mov_b32_e32 v41, v225
	v_mov_b32_e32 v42, v226
	v_mov_b32_e32 v43, v227
	v_mov_b32_e32 v44, v228
	v_mov_b32_e32 v45, v229
	v_mov_b32_e32 v46, v230
	v_mov_b32_e32 v47, v231
	v_mov_b32_e32 v48, v224
	v_mov_b32_e32 v49, v225
	v_mov_b32_e32 v50, v226
	v_mov_b32_e32 v51, v227
	v_mov_b32_e32 v52, v228
	v_mov_b32_e32 v53, v229
	v_mov_b32_e32 v54, v230
	v_mov_b32_e32 v55, v231
	v_mov_b32_e32 v56, v224
	v_mov_b32_e32 v57, v225
	v_mov_b32_e32 v58, v226
	v_mov_b32_e32 v59, v227
	v_mov_b32_e32 v60, v228
	v_mov_b32_e32 v61, v229
	v_mov_b32_e32 v62, v230
	v_mov_b32_e32 v63, v231
	v_mov_b32_e32 v64, v224
	v_mov_b32_e32 v65, v225
	v_mov_b32_e32 v66, v226
	v_mov_b32_e32 v67, v227
	v_add_f32_e32 v68, 1.0, v236
	v_add_f32_e32 v69, 1.0, v237
	v_add_f32_e32 v70, 1.0, v238
	v_add_f32_e32 v71, 1.0, v239
	v_add_f32_e32 v72, 1.0, v232
	v_add_f32_e32 v73, 1.0, v233
	v_add_f32_e32 v74, 1.0, v234
	v_add_f32_e32 v75, 1.0, v235
	v_add_f32_e32 v76, 1.0, v236
	v_add_f32_e32 v77, 1.0, v237
	v_add_f32_e32 v78, 1.0, v238
	v_add_f32_e32 v79, 1.0, v239
	v_add_f32_e32 v80, 1.0, v232
	v_add_f32_e32 v81, 1.0, v233
	v_add_f32_e32 v82, 1.0, v234
	v_add_f32_e32 v83, 1.0, v235
	v_add_f32_e32 v84, 1.0, v236
	v_add_f32_e32 v85, 1.0, v237
	v_add_f32_e32 v86, 1.0, v238
	v_add_f32_e32 v87, 1.0, v239
	v_add_f32_e32 v88, 1.0, v232
	v_add_f32_e32 v89, 1.0, v233
	v_add_f32_e32 v90, 1.0, v234
	v_add_f32_e32 v91, 1.0, v235
	v_add_f32_e32 v92, 1.0, v236
	v_add_f32_e32 v93, 1.0, v237
	v_add_f32_e32 v94, 1.0, v238
	v_add_f32_e32 v95, 1.0, v239
	v_add_f32_e32 v96, 1.0, v232
	v_add_f32_e32 v97, 1.0, v233
	v_add_f32_e32 v98, 1.0, v234
	v_add_f32_e32 v99, 1.0, v235
	v_mov_b32_e32 v100, v228
	v_mov_b32_e32 v101, v229
	v_mov_b32_e32 v102, v230
	v_mov_b32_e32 v103, v231
	v_mov_b32_e32 v104, v224
	v_mov_b32_e32 v105, v225
	v_mov_b32_e32 v106, v226
	v_mov_b32_e32 v107, v227
	v_mov_b32_e32 v108, v228
	v_mov_b32_e32 v109, v229
	v_mov_b32_e32 v110, v230
	v_mov_b32_e32 v111, v231
	v_mov_b32_e32 v112, v224
	v_mov_b32_e32 v113, v225
	v_mov_b32_e32 v114, v226
	v_mov_b32_e32 v115, v227
	v_mov_b32_e32 v116, v228
	v_mov_b32_e32 v117, v229
	v_mov_b32_e32 v118, v230
	v_mov_b32_e32 v119, v231
	v_mov_b32_e32 v120, v224
	v_mov_b32_e32 v121, v225
	v_mov_b32_e32 v122, v226
	v_mov_b32_e32 v123, v227
	v_mov_b32_e32 v124, v228
	v_mov_b32_e32 v125, v229
	v_mov_b32_e32 v126, v230
	v_mov_b32_e32 v127, v231
	v_mov_b32_e32 v128, v224
	v_mov_b32_e32 v129, v225
	v_mov_b32_e32 v130, v226
	v_mov_b32_e32 v131, v227
	s_mov_b32 s76, s77
	s_andn2_b64 vcc, exec, s[38:39]
	s_cbranch_vccz .LBB0_1723

; __device__ __forceinline__ unsigned cvt_pk_bf16(float lo, float hi) { unsigned r; asm volatile("v_cvt_pk_bf16_f32 %0, %1, %2" : "=v"(r) : "v"(lo), "v"(hi)); return r; }
;     __device__ __forceinline__ void operator()(const pg8::f32x4 (&acc)[2][2][4][2], const pg8::Unit& u, int wr, int wc, int fr, int fq) const {
;     ...
;         for (int ai = 0; ai < 2; ++ai)
; #pragma unroll
;             for (int m = 0; m < 4; ++m) {
;                 const int row = u.pm + ai * 128 + wr * 64 + m * 16 + fr;
;                 float a[8];
; #pragma unroll
;                 for (int n = 0; n < 2; ++n)
; #pragma unroll
;                     for (int j = 0; j < 4; ++j) {
;                         const float g = fminf(acc[ai][0][m][n][j] + bgv[n][j], 7.f);
;                         const float l = fminf(fmaxf(acc[ai][1][m][n][j] + blv[n][j], -7.f), 7.f);
;                         const float sg = __builtin_amdgcn_rcpf(1.f + __builtin_amdgcn_exp2f(-1.702f * 1.4426950408889634f * g));
;                         a[n * 4 + j] = g * sg * (l + 1.f);
;                     }
;                 pg8::u32x4 w; w.x = pg8::cvt_pk_bf16(a[0], a[1]); w.y = pg8::cvt_pk_bf16(a[2], a[3]); w.z = pg8::cvt_pk_bf16(a[4], a[5]); w.w = pg8::cvt_pk_bf16(a[6], a[7]);
;                 *(pg8::u32x4*)(ACT + (size_t)row * 1024 + colj) = w;
;             }
.Lup_epi_nonext:
	s_andn2_b64 vcc, exec, s[44:45]
	s_mov_b32 s4, 0xc0c00000
	v_mov_b32_e32 v198, 0x41000000
	v_min_f32_e32 v132, 0x40e00000, v128
	v_min_f32_e32 v133, 0x40e00000, v129
	v_min_f32_e32 v134, 0x40e00000, v130
	v_min_f32_e32 v135, 0x40e00000, v131
	v_min_f32_e32 v136, 0x40e00000, v124
	v_min_f32_e32 v137, 0x40e00000, v125
	v_min_f32_e32 v138, 0x40e00000, v126
	v_min_f32_e32 v139, 0x40e00000, v127
	v_mul_f32_e32 v140, 0xc01d265f, v132
	v_mul_f32_e32 v141, 0xc01d265f, v133
	v_mul_f32_e32 v142, 0xc01d265f, v134
	v_mul_f32_e32 v143, 0xc01d265f, v135
	v_mul_f32_e32 v144, 0xc01d265f, v136
	v_mul_f32_e32 v145, 0xc01d265f, v137
	v_mul_f32_e32 v146, 0xc01d265f, v138
	v_mul_f32_e32 v147, 0xc01d265f, v139
	v_exp_f32_e32 v140, v140
	v_exp_f32_e32 v141, v141
	v_exp_f32_e32 v142, v142
	v_exp_f32_e32 v143, v143
	v_exp_f32_e32 v144, v144
	v_exp_f32_e32 v145, v145
	v_exp_f32_e32 v146, v146
	v_exp_f32_e32 v147, v147
	v_med3_f32 v182, v96, s4, v198
	v_med3_f32 v183, v97, s4, v198
	v_med3_f32 v184, v98, s4, v198
	v_med3_f32 v185, v99, s4, v198
	v_med3_f32 v186, v92, s4, v198
	v_med3_f32 v187, v93, s4, v198
	v_med3_f32 v188, v94, s4, v198
	v_med3_f32 v189, v95, s4, v198
	v_add_f32_e32 v140, 1.0, v140
	v_add_f32_e32 v141, 1.0, v141
	v_add_f32_e32 v142, 1.0, v142
	v_add_f32_e32 v143, 1.0, v143
	v_add_f32_e32 v144, 1.0, v144
	v_add_f32_e32 v145, 1.0, v145
	v_add_f32_e32 v146, 1.0, v146
	v_add_f32_e32 v147, 1.0, v147
	v_rcp_f32_e32 v140, v140
	v_rcp_f32_e32 v141, v141
	v_rcp_f32_e32 v142, v142
	v_rcp_f32_e32 v143, v143
	v_rcp_f32_e32 v144, v144
	v_rcp_f32_e32 v145, v145
	v_rcp_f32_e32 v146, v146
	v_rcp_f32_e32 v147, v147
	v_mul_f32_e32 v132, v132, v182
	v_mul_f32_e32 v133, v133, v183
	v_mul_f32_e32 v134, v134, v184
	v_mul_f32_e32 v135, v135, v185
	v_mul_f32_e32 v136, v136, v186
	v_mul_f32_e32 v137, v137, v187
	v_mul_f32_e32 v138, v138, v188
	v_mul_f32_e32 v139, v139, v189
	v_add_u32_e32 v196, s48, v169
	v_ashrrev_i32_e32 v197, 31, v196
	v_lshlrev_b64 v[194:195], 11, v[196:197]
	v_lshl_add_u64 v[194:195], s[90:91], 0, v[194:195]
	v_lshl_add_u64 v[194:195], v[194:195], 0, v[160:161]
	v_mul_f32_e32 v132, v132, v140
	v_mul_f32_e32 v133, v133, v141
	v_mul_f32_e32 v134, v134, v142
	v_mul_f32_e32 v135, v135, v143
	v_mul_f32_e32 v136, v136, v144
	v_mul_f32_e32 v137, v137, v145
	v_mul_f32_e32 v138, v138, v146
	v_mul_f32_e32 v139, v139, v147
	v_cvt_pk_bf16_f32 v190, v132, v133
	v_cvt_pk_bf16_f32 v191, v134, v135
	v_cvt_pk_bf16_f32 v192, v136, v137
	v_cvt_pk_bf16_f32 v193, v138, v139
	global_store_dwordx4 v[194:195], v[190:193], off
	v_min_f32_e32 v132, 0x40e00000, v120
	v_min_f32_e32 v133, 0x40e00000, v121
	v_min_f32_e32 v134, 0x40e00000, v122
	v_min_f32_e32 v135, 0x40e00000, v123
	v_min_f32_e32 v136, 0x40e00000, v116
	v_min_f32_e32 v137, 0x40e00000, v117
	v_min_f32_e32 v138, 0x40e00000, v118
	v_min_f32_e32 v139, 0x40e00000, v119
	v_mul_f32_e32 v140, 0xc01d265f, v132
	v_mul_f32_e32 v141, 0xc01d265f, v133
	v_mul_f32_e32 v142, 0xc01d265f, v134
	v_mul_f32_e32 v143, 0xc01d265f, v135
	v_mul_f32_e32 v144, 0xc01d265f, v136
	v_mul_f32_e32 v145, 0xc01d265f, v137
	v_mul_f32_e32 v146, 0xc01d265f, v138
	v_mul_f32_e32 v147, 0xc01d265f, v139
	v_exp_f32_e32 v140, v140
	v_exp_f32_e32 v141, v141
	v_exp_f32_e32 v142, v142
	v_exp_f32_e32 v143, v143
	v_exp_f32_e32 v144, v144
	v_exp_f32_e32 v145, v145
	v_exp_f32_e32 v146, v146
	v_exp_f32_e32 v147, v147
	v_med3_f32 v182, v88, s4, v198
	v_med3_f32 v183, v89, s4, v198
	v_med3_f32 v184, v90, s4, v198
	v_med3_f32 v185, v91, s4, v198
	v_med3_f32 v186, v84, s4, v198
	v_med3_f32 v187, v85, s4, v198
	v_med3_f32 v188, v86, s4, v198
	v_med3_f32 v189, v87, s4, v198
	v_add_f32_e32 v140, 1.0, v140
	v_add_f32_e32 v141, 1.0, v141
	v_add_f32_e32 v142, 1.0, v142
	v_add_f32_e32 v143, 1.0, v143
	v_add_f32_e32 v144, 1.0, v144
	v_add_f32_e32 v145, 1.0, v145
	v_add_f32_e32 v146, 1.0, v146
	v_add_f32_e32 v147, 1.0, v147
	v_rcp_f32_e32 v140, v140
	v_rcp_f32_e32 v141, v141
	v_rcp_f32_e32 v142, v142
	v_rcp_f32_e32 v143, v143
	v_rcp_f32_e32 v144, v144
	v_rcp_f32_e32 v145, v145
	v_rcp_f32_e32 v146, v146
	v_rcp_f32_e32 v147, v147
	v_mul_f32_e32 v132, v132, v182
	v_mul_f32_e32 v133, v133, v183
	v_mul_f32_e32 v134, v134, v184
	v_mul_f32_e32 v135, v135, v185
	v_mul_f32_e32 v136, v136, v186
	v_mul_f32_e32 v137, v137, v187
	v_mul_f32_e32 v138, v138, v188
	v_mul_f32_e32 v139, v139, v189
	v_add_u32_e32 v196, s48, v151
	v_ashrrev_i32_e32 v197, 31, v196
	v_lshlrev_b64 v[194:195], 11, v[196:197]
	v_lshl_add_u64 v[194:195], s[90:91], 0, v[194:195]
	v_lshl_add_u64 v[194:195], v[194:195], 0, v[160:161]
	v_mul_f32_e32 v132, v132, v140
	v_mul_f32_e32 v133, v133, v141
	v_mul_f32_e32 v134, v134, v142
	v_mul_f32_e32 v135, v135, v143
	v_mul_f32_e32 v136, v136, v144
	v_mul_f32_e32 v137, v137, v145
	v_mul_f32_e32 v138, v138, v146
	v_mul_f32_e32 v139, v139, v147
	v_cvt_pk_bf16_f32 v190, v132, v133
	v_cvt_pk_bf16_f32 v191, v134, v135
	v_cvt_pk_bf16_f32 v192, v136, v137
	v_cvt_pk_bf16_f32 v193, v138, v139
	global_store_dwordx4 v[194:195], v[190:193], off
	v_min_f32_e32 v132, 0x40e00000, v112
	v_min_f32_e32 v133, 0x40e00000, v113
	v_min_f32_e32 v134, 0x40e00000, v114
	v_min_f32_e32 v135, 0x40e00000, v115
	v_min_f32_e32 v136, 0x40e00000, v108
	v_min_f32_e32 v137, 0x40e00000, v109
	v_min_f32_e32 v138, 0x40e00000, v110
	v_min_f32_e32 v139, 0x40e00000, v111
	v_mul_f32_e32 v140, 0xc01d265f, v132
	v_mul_f32_e32 v141, 0xc01d265f, v133
	v_mul_f32_e32 v142, 0xc01d265f, v134
	v_mul_f32_e32 v143, 0xc01d265f, v135
	v_mul_f32_e32 v144, 0xc01d265f, v136
	v_mul_f32_e32 v145, 0xc01d265f, v137
	v_mul_f32_e32 v146, 0xc01d265f, v138
	v_mul_f32_e32 v147, 0xc01d265f, v139
	v_exp_f32_e32 v140, v140
; __device__ __forceinline__ unsigned cvt_pk_bf16(float lo, float hi) { unsigned r; asm volatile("v_cvt_pk_bf16_f32 %0, %1, %2" : "=v"(r) : "v"(lo), "v"(hi)); return r; }
;     __device__ __forceinline__ void operator()(const pg8::f32x4 (&acc)[2][2][4][2], const pg8::Unit& u, int wr, int wc, int fr, int fq) const {
;     ...
;         for (int ai = 0; ai < 2; ++ai)
; #pragma unroll
;             for (int m = 0; m < 4; ++m) {
;                 const int row = u.pm + ai * 128 + wr * 64 + m * 16 + fr;
;                 float a[8];
; #pragma unroll
;                 for (int n = 0; n < 2; ++n)
; #pragma unroll
;                     for (int j = 0; j < 4; ++j) {
;                         const float g = fminf(acc[ai][0][m][n][j] + bgv[n][j], 7.f);
;                         const float l = fminf(fmaxf(acc[ai][1][m][n][j] + blv[n][j], -7.f), 7.f);
;                         const float sg = __builtin_amdgcn_rcpf(1.f + __builtin_amdgcn_exp2f(-1.702f * 1.4426950408889634f * g));
;                         a[n * 4 + j] = g * sg * (l + 1.f);
;                     }
;                 pg8::u32x4 w; w.x = pg8::cvt_pk_bf16(a[0], a[1]); w.y = pg8::cvt_pk_bf16(a[2], a[3]); w.z = pg8::cvt_pk_bf16(a[4], a[5]); w.w = pg8::cvt_pk_bf16(a[6], a[7]);
;                 *(pg8::u32x4*)(ACT + (size_t)row * 1024 + colj) = w;
;             }
	v_exp_f32_e32 v141, v141
	v_exp_f32_e32 v142, v142
	v_exp_f32_e32 v143, v143
	v_exp_f32_e32 v144, v144
	v_exp_f32_e32 v145, v145
	v_exp_f32_e32 v146, v146
	v_exp_f32_e32 v147, v147
	v_med3_f32 v182, v80, s4, v198
	v_med3_f32 v183, v81, s4, v198
	v_med3_f32 v184, v82, s4, v198
	v_med3_f32 v185, v83, s4, v198
	v_med3_f32 v186, v76, s4, v198
	v_med3_f32 v187, v77, s4, v198
	v_med3_f32 v188, v78, s4, v198
	v_med3_f32 v189, v79, s4, v198
	v_add_f32_e32 v140, 1.0, v140
	v_add_f32_e32 v141, 1.0, v141
	v_add_f32_e32 v142, 1.0, v142
	v_add_f32_e32 v143, 1.0, v143
	v_add_f32_e32 v144, 1.0, v144
	v_add_f32_e32 v145, 1.0, v145
	v_add_f32_e32 v146, 1.0, v146
	v_add_f32_e32 v147, 1.0, v147
	v_rcp_f32_e32 v140, v140
	v_rcp_f32_e32 v141, v141
	v_rcp_f32_e32 v142, v142
	v_rcp_f32_e32 v143, v143
	v_rcp_f32_e32 v144, v144
	v_rcp_f32_e32 v145, v145
	v_rcp_f32_e32 v146, v146
	v_rcp_f32_e32 v147, v147
	v_mul_f32_e32 v132, v132, v182
	v_mul_f32_e32 v133, v133, v183
	v_mul_f32_e32 v134, v134, v184
	v_mul_f32_e32 v135, v135, v185
	v_mul_f32_e32 v136, v136, v186
	v_mul_f32_e32 v137, v137, v187
	v_mul_f32_e32 v138, v138, v188
	v_mul_f32_e32 v139, v139, v189
	v_add_u32_e32 v196, s48, v171
	v_ashrrev_i32_e32 v197, 31, v196
	v_lshlrev_b64 v[194:195], 11, v[196:197]
	v_lshl_add_u64 v[194:195], s[90:91], 0, v[194:195]
	v_lshl_add_u64 v[194:195], v[194:195], 0, v[160:161]
	v_mul_f32_e32 v132, v132, v140
	v_mul_f32_e32 v133, v133, v141
	v_mul_f32_e32 v134, v134, v142
	v_mul_f32_e32 v135, v135, v143
	v_mul_f32_e32 v136, v136, v144
	v_mul_f32_e32 v137, v137, v145
	v_mul_f32_e32 v138, v138, v146
	v_mul_f32_e32 v139, v139, v147
	v_cvt_pk_bf16_f32 v190, v132, v133
	v_cvt_pk_bf16_f32 v191, v134, v135
	v_cvt_pk_bf16_f32 v192, v136, v137
	v_cvt_pk_bf16_f32 v193, v138, v139
	global_store_dwordx4 v[194:195], v[190:193], off
	v_min_f32_e32 v132, 0x40e00000, v104
	v_min_f32_e32 v133, 0x40e00000, v105
	v_min_f32_e32 v134, 0x40e00000, v106
	v_min_f32_e32 v135, 0x40e00000, v107
	v_min_f32_e32 v136, 0x40e00000, v100
	v_min_f32_e32 v137, 0x40e00000, v101
	v_min_f32_e32 v138, 0x40e00000, v102
	v_min_f32_e32 v139, 0x40e00000, v103
	v_mul_f32_e32 v140, 0xc01d265f, v132
	v_mul_f32_e32 v141, 0xc01d265f, v133
	v_mul_f32_e32 v142, 0xc01d265f, v134
	v_mul_f32_e32 v143, 0xc01d265f, v135
	v_mul_f32_e32 v144, 0xc01d265f, v136
	v_mul_f32_e32 v145, 0xc01d265f, v137
	v_mul_f32_e32 v146, 0xc01d265f, v138
	v_mul_f32_e32 v147, 0xc01d265f, v139
	v_exp_f32_e32 v140, v140
	v_exp_f32_e32 v141, v141
	v_exp_f32_e32 v142, v142
	v_exp_f32_e32 v143, v143
	v_exp_f32_e32 v144, v144
	v_exp_f32_e32 v145, v145
	v_exp_f32_e32 v146, v146
	v_exp_f32_e32 v147, v147
	v_med3_f32 v182, v72, s4, v198
	v_med3_f32 v183, v73, s4, v198
	v_med3_f32 v184, v74, s4, v198
	v_med3_f32 v185, v75, s4, v198
	v_med3_f32 v186, v68, s4, v198
	v_med3_f32 v187, v69, s4, v198
	v_med3_f32 v188, v70, s4, v198
	v_med3_f32 v189, v71, s4, v198
	v_add_f32_e32 v140, 1.0, v140
	v_add_f32_e32 v141, 1.0, v141
	v_add_f32_e32 v142, 1.0, v142
	v_add_f32_e32 v143, 1.0, v143
	v_add_f32_e32 v144, 1.0, v144
	v_add_f32_e32 v145, 1.0, v145
	v_add_f32_e32 v146, 1.0, v146
	v_add_f32_e32 v147, 1.0, v147
	v_rcp_f32_e32 v140, v140
	v_rcp_f32_e32 v141, v141
	v_rcp_f32_e32 v142, v142
	v_rcp_f32_e32 v143, v143
	v_rcp_f32_e32 v144, v144
	v_rcp_f32_e32 v145, v145
	v_rcp_f32_e32 v146, v146
	v_rcp_f32_e32 v147, v147
	v_mul_f32_e32 v132, v132, v182
	v_mul_f32_e32 v133, v133, v183
	v_mul_f32_e32 v134, v134, v184
	v_mul_f32_e32 v135, v135, v185
	v_mul_f32_e32 v136, v136, v186
	v_mul_f32_e32 v137, v137, v187
	v_mul_f32_e32 v138, v138, v188
	v_mul_f32_e32 v139, v139, v189
	v_add_u32_e32 v196, s48, v172
	v_ashrrev_i32_e32 v197, 31, v196
	v_lshlrev_b64 v[194:195], 11, v[196:197]
	v_lshl_add_u64 v[194:195], s[90:91], 0, v[194:195]
	v_lshl_add_u64 v[194:195], v[194:195], 0, v[160:161]
	v_mul_f32_e32 v132, v132, v140
	v_mul_f32_e32 v133, v133, v141
	v_mul_f32_e32 v134, v134, v142
	v_mul_f32_e32 v135, v135, v143
	v_mul_f32_e32 v136, v136, v144
	v_mul_f32_e32 v137, v137, v145
	v_mul_f32_e32 v138, v138, v146
	v_mul_f32_e32 v139, v139, v147
	v_cvt_pk_bf16_f32 v190, v132, v133
	v_cvt_pk_bf16_f32 v191, v134, v135
	v_cvt_pk_bf16_f32 v192, v136, v137
	v_cvt_pk_bf16_f32 v193, v138, v139
	global_store_dwordx4 v[194:195], v[190:193], off
	v_min_f32_e32 v132, 0x40e00000, v64
	v_min_f32_e32 v133, 0x40e00000, v65
	v_min_f32_e32 v134, 0x40e00000, v66
	v_min_f32_e32 v135, 0x40e00000, v67
	v_min_f32_e32 v136, 0x40e00000, v60
	v_min_f32_e32 v137, 0x40e00000, v61
	v_min_f32_e32 v138, 0x40e00000, v62
	v_min_f32_e32 v139, 0x40e00000, v63
	v_mul_f32_e32 v140, 0xc01d265f, v132
	v_mul_f32_e32 v141, 0xc01d265f, v133
	v_mul_f32_e32 v142, 0xc01d265f, v134
	v_mul_f32_e32 v143, 0xc01d265f, v135
	v_mul_f32_e32 v144, 0xc01d265f, v136
	v_mul_f32_e32 v145, 0xc01d265f, v137
	v_mul_f32_e32 v146, 0xc01d265f, v138
	v_mul_f32_e32 v147, 0xc01d265f, v139
	v_exp_f32_e32 v140, v140
	v_exp_f32_e32 v141, v141
	v_exp_f32_e32 v142, v142
	v_exp_f32_e32 v143, v143
	v_exp_f32_e32 v144, v144
	v_exp_f32_e32 v145, v145
	v_exp_f32_e32 v146, v146
	v_exp_f32_e32 v147, v147
	v_med3_f32 v182, v32, s4, v198
	v_med3_f32 v183, v33, s4, v198
	v_med3_f32 v184, v34, s4, v198
	v_med3_f32 v185, v35, s4, v198
	v_med3_f32 v186, v28, s4, v198
	v_med3_f32 v187, v29, s4, v198
	v_med3_f32 v188, v30, s4, v198
	v_med3_f32 v189, v31, s4, v198
	v_add_f32_e32 v140, 1.0, v140
	v_add_f32_e32 v141, 1.0, v141
	v_add_f32_e32 v142, 1.0, v142
	v_add_f32_e32 v143, 1.0, v143
	v_add_f32_e32 v144, 1.0, v144
	v_add_f32_e32 v145, 1.0, v145
	v_add_f32_e32 v146, 1.0, v146
	v_add_f32_e32 v147, 1.0, v147
	v_rcp_f32_e32 v140, v140
	v_rcp_f32_e32 v141, v141
	v_rcp_f32_e32 v142, v142
; __device__ __forceinline__ unsigned cvt_pk_bf16(float lo, float hi) { unsigned r; asm volatile("v_cvt_pk_bf16_f32 %0, %1, %2" : "=v"(r) : "v"(lo), "v"(hi)); return r; }
;     __device__ __forceinline__ void operator()(const pg8::f32x4 (&acc)[2][2][4][2], const pg8::Unit& u, int wr, int wc, int fr, int fq) const {
;     ...
;         for (int ai = 0; ai < 2; ++ai)
; #pragma unroll
;             for (int m = 0; m < 4; ++m) {
;                 const int row = u.pm + ai * 128 + wr * 64 + m * 16 + fr;
;                 float a[8];
; #pragma unroll
;                 for (int n = 0; n < 2; ++n)
; #pragma unroll
;                     for (int j = 0; j < 4; ++j) {
;                         const float g = fminf(acc[ai][0][m][n][j] + bgv[n][j], 7.f);
;                         const float l = fminf(fmaxf(acc[ai][1][m][n][j] + blv[n][j], -7.f), 7.f);
;                         const float sg = __builtin_amdgcn_rcpf(1.f + __builtin_amdgcn_exp2f(-1.702f * 1.4426950408889634f * g));
;                         a[n * 4 + j] = g * sg * (l + 1.f);
;                     }
;                 pg8::u32x4 w; w.x = pg8::cvt_pk_bf16(a[0], a[1]); w.y = pg8::cvt_pk_bf16(a[2], a[3]); w.z = pg8::cvt_pk_bf16(a[4], a[5]); w.w = pg8::cvt_pk_bf16(a[6], a[7]);
;                 *(pg8::u32x4*)(ACT + (size_t)row * 1024 + colj) = w;
;             }
	v_rcp_f32_e32 v143, v143
	v_rcp_f32_e32 v144, v144
	v_rcp_f32_e32 v145, v145
	v_rcp_f32_e32 v146, v146
	v_rcp_f32_e32 v147, v147
	v_mul_f32_e32 v132, v132, v182
	v_mul_f32_e32 v133, v133, v183
	v_mul_f32_e32 v134, v134, v184
	v_mul_f32_e32 v135, v135, v185
	v_mul_f32_e32 v136, v136, v186
	v_mul_f32_e32 v137, v137, v187
	v_mul_f32_e32 v138, v138, v188
	v_mul_f32_e32 v139, v139, v189
	v_add_u32_e32 v196, s48, v173
	v_ashrrev_i32_e32 v197, 31, v196
	v_lshlrev_b64 v[194:195], 11, v[196:197]
	v_lshl_add_u64 v[194:195], s[90:91], 0, v[194:195]
	v_lshl_add_u64 v[194:195], v[194:195], 0, v[160:161]
	v_mul_f32_e32 v132, v132, v140
	v_mul_f32_e32 v133, v133, v141
	v_mul_f32_e32 v134, v134, v142
	v_mul_f32_e32 v135, v135, v143
	v_mul_f32_e32 v136, v136, v144
	v_mul_f32_e32 v137, v137, v145
	v_mul_f32_e32 v138, v138, v146
	v_mul_f32_e32 v139, v139, v147
	v_cvt_pk_bf16_f32 v190, v132, v133
	v_cvt_pk_bf16_f32 v191, v134, v135
	v_cvt_pk_bf16_f32 v192, v136, v137
	v_cvt_pk_bf16_f32 v193, v138, v139
	global_store_dwordx4 v[194:195], v[190:193], off
	v_min_f32_e32 v132, 0x40e00000, v56
	v_min_f32_e32 v133, 0x40e00000, v57
	v_min_f32_e32 v134, 0x40e00000, v58
	v_min_f32_e32 v135, 0x40e00000, v59
	v_min_f32_e32 v136, 0x40e00000, v52
	v_min_f32_e32 v137, 0x40e00000, v53
	v_min_f32_e32 v138, 0x40e00000, v54
	v_min_f32_e32 v139, 0x40e00000, v55
	v_mul_f32_e32 v140, 0xc01d265f, v132
	v_mul_f32_e32 v141, 0xc01d265f, v133
	v_mul_f32_e32 v142, 0xc01d265f, v134
	v_mul_f32_e32 v143, 0xc01d265f, v135
	v_mul_f32_e32 v144, 0xc01d265f, v136
	v_mul_f32_e32 v145, 0xc01d265f, v137
	v_mul_f32_e32 v146, 0xc01d265f, v138
	v_mul_f32_e32 v147, 0xc01d265f, v139
	v_exp_f32_e32 v140, v140
	v_exp_f32_e32 v141, v141
	v_exp_f32_e32 v142, v142
	v_exp_f32_e32 v143, v143
	v_exp_f32_e32 v144, v144
	v_exp_f32_e32 v145, v145
	v_exp_f32_e32 v146, v146
	v_exp_f32_e32 v147, v147
	v_med3_f32 v182, v24, s4, v198
	v_med3_f32 v183, v25, s4, v198
	v_med3_f32 v184, v26, s4, v198
	v_med3_f32 v185, v27, s4, v198
	v_med3_f32 v186, v20, s4, v198
	v_med3_f32 v187, v21, s4, v198
	v_med3_f32 v188, v22, s4, v198
	v_med3_f32 v189, v23, s4, v198
	v_add_f32_e32 v140, 1.0, v140
	v_add_f32_e32 v141, 1.0, v141
	v_add_f32_e32 v142, 1.0, v142
	v_add_f32_e32 v143, 1.0, v143
	v_add_f32_e32 v144, 1.0, v144
	v_add_f32_e32 v145, 1.0, v145
	v_add_f32_e32 v146, 1.0, v146
	v_add_f32_e32 v147, 1.0, v147
	v_rcp_f32_e32 v140, v140
	v_rcp_f32_e32 v141, v141
	v_rcp_f32_e32 v142, v142
	v_rcp_f32_e32 v143, v143
	v_rcp_f32_e32 v144, v144
	v_rcp_f32_e32 v145, v145
	v_rcp_f32_e32 v146, v146
	v_rcp_f32_e32 v147, v147
	v_mul_f32_e32 v132, v132, v182
	v_mul_f32_e32 v133, v133, v183
	v_mul_f32_e32 v134, v134, v184
	v_mul_f32_e32 v135, v135, v185
	v_mul_f32_e32 v136, v136, v186
	v_mul_f32_e32 v137, v137, v187
	v_mul_f32_e32 v138, v138, v188
	v_mul_f32_e32 v139, v139, v189
	v_add_u32_e32 v196, s48, v174
	v_ashrrev_i32_e32 v197, 31, v196
	v_lshlrev_b64 v[194:195], 11, v[196:197]
	v_lshl_add_u64 v[194:195], s[90:91], 0, v[194:195]
	v_lshl_add_u64 v[194:195], v[194:195], 0, v[160:161]
	v_mul_f32_e32 v132, v132, v140
	v_mul_f32_e32 v133, v133, v141
	v_mul_f32_e32 v134, v134, v142
	v_mul_f32_e32 v135, v135, v143
	v_mul_f32_e32 v136, v136, v144
	v_mul_f32_e32 v137, v137, v145
	v_mul_f32_e32 v138, v138, v146
	v_mul_f32_e32 v139, v139, v147
	v_cvt_pk_bf16_f32 v190, v132, v133
	v_cvt_pk_bf16_f32 v191, v134, v135
	v_cvt_pk_bf16_f32 v192, v136, v137
	v_cvt_pk_bf16_f32 v193, v138, v139
	global_store_dwordx4 v[194:195], v[190:193], off
	v_min_f32_e32 v132, 0x40e00000, v48
	v_min_f32_e32 v133, 0x40e00000, v49
	v_min_f32_e32 v134, 0x40e00000, v50
	v_min_f32_e32 v135, 0x40e00000, v51
	v_min_f32_e32 v136, 0x40e00000, v44
	v_min_f32_e32 v137, 0x40e00000, v45
	v_min_f32_e32 v138, 0x40e00000, v46
	v_min_f32_e32 v139, 0x40e00000, v47
	v_mul_f32_e32 v140, 0xc01d265f, v132
	v_mul_f32_e32 v141, 0xc01d265f, v133
	v_mul_f32_e32 v142, 0xc01d265f, v134
	v_mul_f32_e32 v143, 0xc01d265f, v135
	v_mul_f32_e32 v144, 0xc01d265f, v136
	v_mul_f32_e32 v145, 0xc01d265f, v137
	v_mul_f32_e32 v146, 0xc01d265f, v138
	v_mul_f32_e32 v147, 0xc01d265f, v139
	v_exp_f32_e32 v140, v140
	v_exp_f32_e32 v141, v141
	v_exp_f32_e32 v142, v142
	v_exp_f32_e32 v143, v143
	v_exp_f32_e32 v144, v144
	v_exp_f32_e32 v145, v145
; __device__ __forceinline__ unsigned cvt_pk_bf16(float lo, float hi) { unsigned r; asm volatile("v_cvt_pk_bf16_f32 %0, %1, %2" : "=v"(r) : "v"(lo), "v"(hi)); return r; }
; template <class Epi, class Sched, bool ALIGN_EPI = false, bool SP2 = false, bool GATHER = false, bool HALFM = false>
; __device__ __forceinline__ void gemm_phase(PG8_LAS unsigned char* lds, const int Kdim, const Sched& S, const Epi& E) {
;     ...
;         if (!has_next) break;
;     __device__ __forceinline__ void operator()(const pg8::f32x4 (&acc)[2][2][4][2], const pg8::Unit& u, int wr, int wc, int fr, int fq) const {
;     ...
;         for (int ai = 0; ai < 2; ++ai)
; #pragma unroll
;             for (int m = 0; m < 4; ++m) {
;                 const int row = u.pm + ai * 128 + wr * 64 + m * 16 + fr;
;                 float a[8];
; #pragma unroll
;                 for (int n = 0; n < 2; ++n)
; #pragma unroll
;                     for (int j = 0; j < 4; ++j) {
;                         const float g = fminf(acc[ai][0][m][n][j] + bgv[n][j], 7.f);
;                         const float l = fminf(fmaxf(acc[ai][1][m][n][j] + blv[n][j], -7.f), 7.f);
;                         const float sg = __builtin_amdgcn_rcpf(1.f + __builtin_amdgcn_exp2f(-1.702f * 1.4426950408889634f * g));
;                         a[n * 4 + j] = g * sg * (l + 1.f);
;                     }
;                 pg8::u32x4 w; w.x = pg8::cvt_pk_bf16(a[0], a[1]); w.y = pg8::cvt_pk_bf16(a[2], a[3]); w.z = pg8::cvt_pk_bf16(a[4], a[5]); w.w = pg8::cvt_pk_bf16(a[6], a[7]);
;                 *(pg8::u32x4*)(ACT + (size_t)row * 1024 + colj) = w;
;             }
	v_exp_f32_e32 v146, v146
	v_exp_f32_e32 v147, v147
	v_med3_f32 v182, v16, s4, v198
	v_med3_f32 v183, v17, s4, v198
	v_med3_f32 v184, v18, s4, v198
	v_med3_f32 v185, v19, s4, v198
	v_med3_f32 v186, v12, s4, v198
	v_med3_f32 v187, v13, s4, v198
	v_med3_f32 v188, v14, s4, v198
	v_med3_f32 v189, v15, s4, v198
	v_add_f32_e32 v140, 1.0, v140
	v_add_f32_e32 v141, 1.0, v141
	v_add_f32_e32 v142, 1.0, v142
	v_add_f32_e32 v143, 1.0, v143
	v_add_f32_e32 v144, 1.0, v144
	v_add_f32_e32 v145, 1.0, v145
	v_add_f32_e32 v146, 1.0, v146
	v_add_f32_e32 v147, 1.0, v147
	v_rcp_f32_e32 v140, v140
	v_rcp_f32_e32 v141, v141
	v_rcp_f32_e32 v142, v142
	v_rcp_f32_e32 v143, v143
	v_rcp_f32_e32 v144, v144
	v_rcp_f32_e32 v145, v145
	v_rcp_f32_e32 v146, v146
	v_rcp_f32_e32 v147, v147
	v_mul_f32_e32 v132, v132, v182
	v_mul_f32_e32 v133, v133, v183
	v_mul_f32_e32 v134, v134, v184
	v_mul_f32_e32 v135, v135, v185
	v_mul_f32_e32 v136, v136, v186
	v_mul_f32_e32 v137, v137, v187
	v_mul_f32_e32 v138, v138, v188
	v_mul_f32_e32 v139, v139, v189
	v_add_u32_e32 v196, s48, v175
	v_ashrrev_i32_e32 v197, 31, v196
	v_lshlrev_b64 v[194:195], 11, v[196:197]
	v_lshl_add_u64 v[194:195], s[90:91], 0, v[194:195]
	v_lshl_add_u64 v[194:195], v[194:195], 0, v[160:161]
	v_mul_f32_e32 v132, v132, v140
	v_mul_f32_e32 v133, v133, v141
	v_mul_f32_e32 v134, v134, v142
	v_mul_f32_e32 v135, v135, v143
	v_mul_f32_e32 v136, v136, v144
	v_mul_f32_e32 v137, v137, v145
	v_mul_f32_e32 v138, v138, v146
	v_mul_f32_e32 v139, v139, v147
	v_cvt_pk_bf16_f32 v190, v132, v133
	v_cvt_pk_bf16_f32 v191, v134, v135
	v_cvt_pk_bf16_f32 v192, v136, v137
	v_cvt_pk_bf16_f32 v193, v138, v139
	global_store_dwordx4 v[194:195], v[190:193], off
	v_min_f32_e32 v132, 0x40e00000, v40
	v_min_f32_e32 v133, 0x40e00000, v41
	v_min_f32_e32 v134, 0x40e00000, v42
	v_min_f32_e32 v135, 0x40e00000, v43
	v_min_f32_e32 v136, 0x40e00000, v36
	v_min_f32_e32 v137, 0x40e00000, v37
	v_min_f32_e32 v138, 0x40e00000, v38
	v_min_f32_e32 v139, 0x40e00000, v39
	v_mul_f32_e32 v140, 0xc01d265f, v132
	v_mul_f32_e32 v141, 0xc01d265f, v133
	v_mul_f32_e32 v142, 0xc01d265f, v134
	v_mul_f32_e32 v143, 0xc01d265f, v135
	v_mul_f32_e32 v144, 0xc01d265f, v136
	v_mul_f32_e32 v145, 0xc01d265f, v137
	v_mul_f32_e32 v146, 0xc01d265f, v138
	v_mul_f32_e32 v147, 0xc01d265f, v139
	v_exp_f32_e32 v140, v140
	v_exp_f32_e32 v141, v141
	v_exp_f32_e32 v142, v142
	v_exp_f32_e32 v143, v143
	v_exp_f32_e32 v144, v144
	v_exp_f32_e32 v145, v145
	v_exp_f32_e32 v146, v146
	v_exp_f32_e32 v147, v147
	v_med3_f32 v182, v8, s4, v198
	v_med3_f32 v183, v9, s4, v198
	v_med3_f32 v184, v10, s4, v198
	v_med3_f32 v185, v11, s4, v198
	v_med3_f32 v186, v4, s4, v198
	v_med3_f32 v187, v5, s4, v198
	v_med3_f32 v188, v6, s4, v198
	v_med3_f32 v189, v7, s4, v198
	v_add_f32_e32 v140, 1.0, v140
	v_add_f32_e32 v141, 1.0, v141
	v_add_f32_e32 v142, 1.0, v142
	v_add_f32_e32 v143, 1.0, v143
	v_add_f32_e32 v144, 1.0, v144
	v_add_f32_e32 v145, 1.0, v145
	v_add_f32_e32 v146, 1.0, v146
	v_add_f32_e32 v147, 1.0, v147
	v_rcp_f32_e32 v140, v140
	v_rcp_f32_e32 v141, v141
	v_rcp_f32_e32 v142, v142
	v_rcp_f32_e32 v143, v143
	v_rcp_f32_e32 v144, v144
	v_rcp_f32_e32 v145, v145
	v_rcp_f32_e32 v146, v146
	v_rcp_f32_e32 v147, v147
	v_mul_f32_e32 v132, v132, v182
	v_mul_f32_e32 v133, v133, v183
	v_mul_f32_e32 v134, v134, v184
	v_mul_f32_e32 v135, v135, v185
	v_mul_f32_e32 v136, v136, v186
	v_mul_f32_e32 v137, v137, v187
	v_mul_f32_e32 v138, v138, v188
	v_mul_f32_e32 v139, v139, v189
	v_add_u32_e32 v196, s48, v176
	v_ashrrev_i32_e32 v197, 31, v196
	v_lshlrev_b64 v[194:195], 11, v[196:197]
	v_lshl_add_u64 v[194:195], s[90:91], 0, v[194:195]
	v_lshl_add_u64 v[194:195], v[194:195], 0, v[160:161]
	v_mul_f32_e32 v132, v132, v140
	v_mul_f32_e32 v133, v133, v141
	v_mul_f32_e32 v134, v134, v142
	v_mul_f32_e32 v135, v135, v143
	v_mul_f32_e32 v136, v136, v144
	v_mul_f32_e32 v137, v137, v145
	v_mul_f32_e32 v138, v138, v146
	v_mul_f32_e32 v139, v139, v147
	v_cvt_pk_bf16_f32 v190, v132, v133
	v_cvt_pk_bf16_f32 v191, v134, v135
	v_cvt_pk_bf16_f32 v192, v136, v137
	v_cvt_pk_bf16_f32 v193, v138, v139
	global_store_dwordx4 v[194:195], v[190:193], off
	s_cbranch_vccnz .LBB0_1722
	v_readlane_b32 s82, v255, 1
	v_readlane_b32 s83, v255, 2
	s_branch .LBB0_1697
